# W12 with the grid-barrier spin loops polling back-to-back (s_sleep 0 instead of s_sleep 1)
# speedup vs baseline: 1.0035x; 1.0035x over previous
.LBB0_107:
	global_load_dword v15, v16, s[8:9] sc1
	global_load_dword v0, v16, s[10:11] sc1
	global_load_dword v1, v16, s[12:13] sc1
	global_load_dword v2, v16, s[14:15] sc1
	global_load_dword v3, v16, s[16:17] sc1
	global_load_dword v4, v16, s[18:19] sc1
	global_load_dword v5, v16, s[20:21] sc1
	global_load_dword v6, v16, s[22:23] sc1
	global_load_dword v7, v16, s[24:25] sc1
	global_load_dword v8, v16, s[26:27] sc1
	global_load_dword v9, v16, s[30:31] sc1
	global_load_dword v10, v16, s[34:35] sc1
	global_load_dword v11, v16, s[36:37] sc1
	global_load_dword v12, v16, s[38:39] sc1
	global_load_dword v13, v16, s[2:3] sc1
	global_load_dword v14, v16, s[40:41] sc1
	s_mov_b64 s[42:43], -1
	s_mov_b64 s[44:45], -1
	s_waitcnt vmcnt(14)
	v_add_u32_e32 v17, v0, v15
	s_waitcnt vmcnt(13)
	v_add_u32_e32 v17, v17, v1
	s_waitcnt vmcnt(12)
	v_add_u32_e32 v17, v17, v2
	s_waitcnt vmcnt(11)
	v_add_u32_e32 v17, v17, v3
	s_waitcnt vmcnt(10)
	v_add_u32_e32 v17, v17, v4
	s_waitcnt vmcnt(9)
	v_add_u32_e32 v17, v17, v5
	s_waitcnt vmcnt(8)
	v_add_u32_e32 v17, v17, v6
	s_waitcnt vmcnt(7)
	v_add_u32_e32 v17, v17, v7
	s_waitcnt vmcnt(6)
	v_add_u32_e32 v17, v17, v8
	s_waitcnt vmcnt(5)
	v_add_u32_e32 v17, v17, v9
	s_waitcnt vmcnt(4)
	v_add_u32_e32 v17, v17, v10
	s_waitcnt vmcnt(3)
	v_add_u32_e32 v17, v17, v11
	s_waitcnt vmcnt(2)
	v_add_u32_e32 v17, v17, v12
	s_waitcnt vmcnt(1)
	v_add_u32_e32 v17, v17, v13
	s_waitcnt vmcnt(0)
	v_add_u32_e32 v17, v17, v14
	v_cmp_eq_u32_e32 vcc, s29, v17
	s_cbranch_vccnz .LBB0_106
	s_and_b32 s42, s33, 0xff
	s_cmp_eq_u32 s42, 0
	s_mov_b64 s[42:43], -1
	s_mov_b64 s[46:47], -1
	s_sleep 0
	s_cbranch_scc1 .LBB0_111
	s_and_b64 vcc, exec, s[46:47]
	s_cbranch_vccz .LBB0_106

.LBB0_123:
	s_and_b32 s18, s22, 0xff
	s_mov_b64 s[16:17], -1
	s_cmp_lg_u32 s18, 0
	s_mov_b64 s[20:21], -1
	s_sleep 0
	s_cbranch_scc0 .LBB0_126
	s_and_b64 vcc, exec, s[20:21]
	s_cbranch_vccz .LBB0_122

.LBB0_140:
	s_and_b32 s18, s24, 0xff
	s_cmp_lg_u32 s18, 0
	s_mov_b64 s[20:21], -1
	s_sleep 0
	s_cbranch_scc0 .LBB0_143
	s_mov_b64 s[22:23], -1
	s_and_b64 vcc, exec, s[20:21]
	s_cbranch_vccz .LBB0_139

.LBB0_165:
	global_load_dword v15, v16, s[8:9] sc1
	global_load_dword v0, v16, s[10:11] sc1
	global_load_dword v1, v16, s[12:13] sc1
	global_load_dword v2, v16, s[14:15] sc1
	global_load_dword v3, v16, s[16:17] sc1
	global_load_dword v4, v16, s[18:19] sc1
	global_load_dword v5, v16, s[20:21] sc1
	global_load_dword v6, v16, s[22:23] sc1
	global_load_dword v7, v16, s[24:25] sc1
	global_load_dword v8, v16, s[26:27] sc1
	global_load_dword v9, v16, s[30:31] sc1
	global_load_dword v10, v16, s[34:35] sc1
	global_load_dword v11, v16, s[36:37] sc1
	global_load_dword v12, v16, s[38:39] sc1
	global_load_dword v13, v16, s[6:7] sc1
	global_load_dword v14, v16, s[40:41] sc1
	s_mov_b64 s[42:43], -1
	s_mov_b64 s[44:45], -1
	s_waitcnt vmcnt(14)
	v_add_u32_e32 v17, v0, v15
	s_waitcnt vmcnt(13)
	v_add_u32_e32 v17, v17, v1
	s_waitcnt vmcnt(12)
	v_add_u32_e32 v17, v17, v2
	s_waitcnt vmcnt(11)
	v_add_u32_e32 v17, v17, v3
	s_waitcnt vmcnt(10)
	v_add_u32_e32 v17, v17, v4
	s_waitcnt vmcnt(9)
	v_add_u32_e32 v17, v17, v5
	s_waitcnt vmcnt(8)
	v_add_u32_e32 v17, v17, v6
	s_waitcnt vmcnt(7)
	v_add_u32_e32 v17, v17, v7
	s_waitcnt vmcnt(6)
	v_add_u32_e32 v17, v17, v8
	s_waitcnt vmcnt(5)
	v_add_u32_e32 v17, v17, v9
	s_waitcnt vmcnt(4)
	v_add_u32_e32 v17, v17, v10
	s_waitcnt vmcnt(3)
	v_add_u32_e32 v17, v17, v11
	s_waitcnt vmcnt(2)
	v_add_u32_e32 v17, v17, v12
	s_waitcnt vmcnt(1)
	v_add_u32_e32 v17, v17, v13
	s_waitcnt vmcnt(0)
	v_add_u32_e32 v17, v17, v14
	v_cmp_eq_u32_e32 vcc, s29, v17
	s_cbranch_vccnz .LBB0_164
	s_and_b32 s42, s33, 0xff
	s_cmp_eq_u32 s42, 0
	s_mov_b64 s[42:43], -1
	s_mov_b64 s[46:47], -1
	s_sleep 0
	s_cbranch_scc1 .LBB0_169
	s_and_b64 vcc, exec, s[46:47]
	s_cbranch_vccz .LBB0_164

.LBB0_225:
	v_readlane_b32 s2, v253, 53
	v_readlane_b32 s3, v253, 54
	s_mov_b64 s[4:5], -1
	s_nop 3
	global_load_dword v0, v213, s[2:3] sc1
	v_readlane_b32 s2, v253, 55
	v_readlane_b32 s3, v253, 56
	s_nop 4
	global_load_dword v1, v213, s[2:3] sc1
	v_readlane_b32 s2, v253, 57
	v_readlane_b32 s3, v253, 58
	s_waitcnt vmcnt(0)
	v_add_u32_e32 v16, v1, v0
	s_nop 2
	global_load_dword v2, v213, s[2:3] sc1
	v_readlane_b32 s2, v253, 59
	v_readlane_b32 s3, v253, 60
	s_waitcnt vmcnt(0)
	v_add_u32_e32 v16, v16, v2
	s_nop 2
	global_load_dword v3, v213, s[2:3] sc1
	v_readlane_b32 s2, v253, 61
	v_readlane_b32 s3, v253, 62
	s_waitcnt vmcnt(0)
	v_add_u32_e32 v16, v16, v3
	s_nop 2
	global_load_dword v4, v213, s[2:3] sc1
	v_readlane_b32 s2, v253, 63
	v_readlane_b32 s3, v254, 0
	s_waitcnt vmcnt(0)
	v_add_u32_e32 v16, v16, v4
	s_nop 2
	global_load_dword v5, v213, s[2:3] sc1
	v_readlane_b32 s2, v254, 1
	v_readlane_b32 s3, v254, 2
	s_waitcnt vmcnt(0)
	v_add_u32_e32 v16, v16, v5
	s_nop 2
	global_load_dword v6, v213, s[2:3] sc1
	v_readlane_b32 s2, v254, 3
	v_readlane_b32 s3, v254, 4
	s_waitcnt vmcnt(0)
	v_add_u32_e32 v16, v16, v6
	s_nop 2
	global_load_dword v7, v213, s[2:3] sc1
	v_readlane_b32 s2, v254, 5
	v_readlane_b32 s3, v254, 6
	s_waitcnt vmcnt(0)
	v_add_u32_e32 v16, v16, v7
	s_nop 2
	global_load_dword v8, v213, s[2:3] sc1
	v_readlane_b32 s2, v254, 7
	v_readlane_b32 s3, v254, 8
	s_waitcnt vmcnt(0)
	v_add_u32_e32 v16, v16, v8
	s_nop 2
	global_load_dword v9, v213, s[2:3] sc1
	v_readlane_b32 s2, v254, 9
	v_readlane_b32 s3, v254, 10
	s_waitcnt vmcnt(0)
	v_add_u32_e32 v16, v16, v9
	s_nop 2
	global_load_dword v10, v213, s[2:3] sc1
	v_readlane_b32 s2, v254, 11
	v_readlane_b32 s3, v254, 12
	s_waitcnt vmcnt(0)
	v_add_u32_e32 v16, v16, v10
	s_nop 2
	global_load_dword v11, v213, s[2:3] sc1
	v_readlane_b32 s2, v254, 13
	v_readlane_b32 s3, v254, 14
	s_waitcnt vmcnt(0)
	v_add_u32_e32 v16, v16, v11
	s_nop 2
	global_load_dword v12, v213, s[2:3] sc1
	v_readlane_b32 s2, v254, 15
	v_readlane_b32 s3, v254, 16
	s_waitcnt vmcnt(0)
	v_add_u32_e32 v16, v16, v12
	s_nop 2
	global_load_dword v13, v213, s[2:3] sc1
	v_readlane_b32 s2, v254, 17
	v_readlane_b32 s3, v254, 18
	s_waitcnt vmcnt(0)
	v_add_u32_e32 v16, v16, v13
	s_nop 2
	global_load_dword v14, v213, s[2:3] sc1
	v_readlane_b32 s2, v254, 19
	v_readlane_b32 s3, v254, 20
	s_waitcnt vmcnt(0)
	v_add_u32_e32 v16, v16, v14
	s_nop 2
	global_load_dword v15, v213, s[2:3] sc1
	s_mov_b64 s[2:3], -1
	s_waitcnt vmcnt(0)
	v_add_u32_e32 v16, v16, v15
	v_cmp_eq_u32_e32 vcc, s8, v16
	s_cbranch_vccnz .LBB0_224
	s_and_b32 s2, s13, 0xff
	s_cmp_eq_u32 s2, 0
	s_mov_b64 s[2:3], -1
	s_mov_b64 s[20:21], -1
	s_sleep 0
	s_cbranch_scc1 .LBB0_229
	s_and_b64 vcc, exec, s[20:21]
	s_cbranch_vccz .LBB0_224

.LBB0_270:
	s_and_b32 s13, s8, 0xff
	s_mov_b64 s[24:25], -1
	s_cmp_lg_u32 s13, 0
	s_mov_b64 s[36:37], -1
	s_sleep 0
	s_cbranch_scc0 .LBB0_273
	s_and_b64 vcc, exec, s[36:37]
	s_cbranch_vccz .LBB0_269
